# v33 + barrier leader tail: per-XCD generation atomic removed (unused), acquire invalidate no longer waits for the top-generation atomic ack
# speedup vs baseline: 1.0144x; 1.0004x over previous
; __device__ __forceinline__ unsigned xb_add(unsigned* p, unsigned v) { return __hip_atomic_fetch_add(p, v, __ATOMIC_RELAXED, __HIP_MEMORY_SCOPE_AGENT); }
; __device__ __forceinline__ void xcd_barrier(const XcdBarrier& b) {
;     ...
;             __builtin_amdgcn_fence(__ATOMIC_ACQUIRE, "agent");
;             xb_add(&bar[XB_XGEN(b.x)], 1u);
;             asm volatile("s_waitcnt vmcnt(0)" ::: "memory");
.LBB0_136:
	s_or_b64 exec, exec, s[0:1]
	s_add_i32 s0, s20, 0x900
	s_mov_b32 s1, 0
	s_lshl_b64 s[0:1], s[0:1], 2
	s_add_u32 s0, s30, s0
	s_addc_u32 s1, s31, s1
	v_mov_b32_e32 v1, 1
	v_mov_b64_e32 v[2:3], s[0:1]
	buffer_inv sc1
	s_waitcnt vmcnt(0)

; __device__ __forceinline__ unsigned xb_add(unsigned* p, unsigned v) { return __hip_atomic_fetch_add(p, v, __ATOMIC_RELAXED, __HIP_MEMORY_SCOPE_AGENT); }
; __device__ __forceinline__ void xcd_barrier(const XcdBarrier& b) {
;     ...
;             __builtin_amdgcn_fence(__ATOMIC_ACQUIRE, "agent");
;             xb_add(&bar[XB_XGEN(b.x)], 1u);
;             asm volatile("s_waitcnt vmcnt(0)" ::: "memory");
.LBB0_643:
	s_or_b64 exec, exec, s[2:3]
	s_add_i32 s68, s1, 0x900
	s_lshl_b64 s[2:3], s[68:69], 2
	s_add_u32 s2, s34, s2
	s_addc_u32 s3, s35, s3
	v_mov_b64_e32 v[4:5], s[2:3]
	buffer_inv sc1
	s_waitcnt vmcnt(0)

; __device__ __forceinline__ unsigned xb_add(unsigned* p, unsigned v) { return __hip_atomic_fetch_add(p, v, __ATOMIC_RELAXED, __HIP_MEMORY_SCOPE_AGENT); }
; __device__ __forceinline__ void xcd_barrier(const XcdBarrier& b) {
;     ...
;             __builtin_amdgcn_fence(__ATOMIC_ACQUIRE, "agent");
;             xb_add(&bar[XB_XGEN(b.x)], 1u);
;             asm volatile("s_waitcnt vmcnt(0)" ::: "memory");
.LBB0_873:
	s_or_b64 exec, exec, s[4:5]
	s_add_i32 s68, s1, 0x900
	s_lshl_b64 s[4:5], s[68:69], 2
	s_add_u32 s4, s40, s4
	s_addc_u32 s5, s41, s5
	v_mov_b64_e32 v[4:5], s[4:5]
	buffer_inv sc1
	s_waitcnt vmcnt(0)

; __device__ __forceinline__ unsigned xb_add(unsigned* p, unsigned v) { return __hip_atomic_fetch_add(p, v, __ATOMIC_RELAXED, __HIP_MEMORY_SCOPE_AGENT); }
; __device__ __forceinline__ void xcd_barrier(const XcdBarrier& b) {
;     ...
;             __builtin_amdgcn_fence(__ATOMIC_ACQUIRE, "agent");
;             xb_add(&bar[XB_XGEN(b.x)], 1u);
;             asm volatile("s_waitcnt vmcnt(0)" ::: "memory");
.LBB0_1071:
	s_or_b64 exec, exec, s[4:5]
	s_add_i32 s68, s1, 0x900
	s_lshl_b64 s[4:5], s[68:69], 2
	s_add_u32 s4, s38, s4
	s_addc_u32 s5, s39, s5
	v_mov_b64_e32 v[4:5], s[4:5]
	buffer_inv sc1
	s_waitcnt vmcnt(0)

; __device__ __forceinline__ unsigned xb_add(unsigned* p, unsigned v) { return __hip_atomic_fetch_add(p, v, __ATOMIC_RELAXED, __HIP_MEMORY_SCOPE_AGENT); }
; __device__ __forceinline__ void xcd_barrier(const XcdBarrier& b) {
;     ...
;             __builtin_amdgcn_fence(__ATOMIC_ACQUIRE, "agent");
;             xb_add(&bar[XB_XGEN(b.x)], 1u);
;             asm volatile("s_waitcnt vmcnt(0)" ::: "memory");
.LBB0_1802:
	s_or_b64 exec, exec, s[2:3]
	s_add_i32 s68, s0, 0x900
	s_lshl_b64 s[0:1], s[68:69], 2
	s_add_u32 s0, s34, s0
	s_addc_u32 s1, s35, s1
	v_mov_b64_e32 v[4:5], s[0:1]
	buffer_inv sc1
	s_waitcnt vmcnt(0)
